# speedup vs baseline: 1.0077x; 1.0077x over previous
.Llight_path:
	s_waitcnt vmcnt(16)
	v_mul_u32_u24_e32 v236, 36, v228
	v_add_u32_e32 v236, v236, v230
	v_add_u32_e32 v237, s7, v229
	v_mul_u32_u24_e32 v238, 0x104, v228
	v_add_u32_e32 v238, v238, v237
	v_add_u32_e32 v238, 0xb840, v238
	v_add_u32_e32 v231, s7, v229
	v_add_u32_e32 v231, 0xb840, v231
	v_add_u32_e32 v211, s6, v210
	s_nop 0
	s_load_dwordx8 s[4:11], s[0:1], 0x10
	v_add_u32_e32 v232, 0x24e80, v228
	ds_read_b32 v244, v232
	ds_read_b32 v245, v232 offset:128
	ds_read_b128 v[194:197], v237 offset:36928
	ds_read_b128 v[198:201], v237 offset:36944
	ds_read_b128 v[202:205], v237 offset:36960
	ds_read_b128 v[206:209], v237 offset:36976
	ds_read_b128 v[212:215], v237 offset:37056
	ds_read_b128 v[216:219], v237 offset:37072
	ds_read_b128 v[220:223], v237 offset:37088
	ds_read_b128 v[224:227], v237 offset:37104
	ds_read_b128 v[162:165], v236 offset:16384
	ds_read_b128 v[166:169], v236 offset:16416
	ds_read_b128 v[170:173], v236 offset:16448
	ds_read_b128 v[174:177], v236 offset:16480
	s_waitcnt lgkmcnt(0)
	v_mfma_f32_32x32x16_bf16 v[2:17], v[94:97], v[162:165], v[194:209]
	v_mfma_f32_32x32x16_bf16 v[18:33], v[46:49], v[162:165], v[212:227]
	v_mfma_f32_32x32x16_bf16 v[2:17], v[90:93], v[166:169], v[2:17]
	v_mfma_f32_32x32x16_bf16 v[18:33], v[42:45], v[166:169], v[18:33]
	v_mfma_f32_32x32x16_bf16 v[2:17], v[86:89], v[170:173], v[2:17]
	ds_read_b128 v[178:181], v236 offset:20992
	v_mfma_f32_32x32x16_bf16 v[18:33], v[38:41], v[170:173], v[18:33]
	ds_read_b128 v[182:185], v236 offset:21024
	v_mfma_f32_32x32x16_bf16 v[2:17], v[82:85], v[174:177], v[2:17]
	ds_read_b128 v[186:189], v236 offset:21056
	v_mfma_f32_32x32x16_bf16 v[18:33], v[34:37], v[174:177], v[18:33]
	ds_read_b128 v[190:193], v236 offset:21088
	s_waitcnt lgkmcnt(0)
	v_mfma_f32_32x32x16_bf16 v[130:145], v[94:97], v[178:181], v[194:209]
	v_mfma_f32_32x32x16_bf16 v[146:161], v[46:49], v[178:181], v[212:227]
	v_mfma_f32_32x32x16_bf16 v[130:145], v[90:93], v[182:185], v[130:145]
	v_mfma_f32_32x32x16_bf16 v[146:161], v[42:45], v[182:185], v[146:161]
	s_nop 7
	ds_write_b128 v238, v[2:5] offset:0
	ds_write_b128 v238, v[6:9] offset:16
	ds_write_b128 v238, v[10:13] offset:32
	ds_write_b128 v238, v[14:17] offset:48
	ds_write_b128 v238, v[18:21] offset:128
	ds_write_b128 v238, v[22:25] offset:144
	ds_write_b128 v238, v[26:29] offset:160
	ds_write_b128 v238, v[30:33] offset:176
	v_mfma_f32_32x32x16_bf16 v[130:145], v[86:89], v[186:189], v[130:145]
	ds_read_b128 v[162:165], v236 offset:25600
	v_mfma_f32_32x32x16_bf16 v[146:161], v[38:41], v[186:189], v[146:161]
	ds_read_b128 v[166:169], v236 offset:25632
	v_mfma_f32_32x32x16_bf16 v[130:145], v[82:85], v[190:193], v[130:145]
	ds_read_b128 v[170:173], v236 offset:25664
	v_mfma_f32_32x32x16_bf16 v[146:161], v[34:37], v[190:193], v[146:161]
	ds_read_b128 v[174:177], v236 offset:25696
	s_waitcnt lgkmcnt(0)
	v_mfma_f32_32x32x16_bf16 v[2:17], v[94:97], v[162:165], v[194:209]
	v_mfma_f32_32x32x16_bf16 v[18:33], v[46:49], v[162:165], v[212:227]
	v_mfma_f32_32x32x16_bf16 v[2:17], v[90:93], v[166:169], v[2:17]
	v_mfma_f32_32x32x16_bf16 v[18:33], v[42:45], v[166:169], v[18:33]
	s_nop 7
	v_add_u32_e32 v239, 0x8200, v238
	ds_write_b128 v239, v[130:133] offset:0
	ds_write_b128 v239, v[134:137] offset:16
	ds_write_b128 v239, v[138:141] offset:32
	ds_write_b128 v239, v[142:145] offset:48
	ds_write_b128 v239, v[146:149] offset:128
	ds_write_b128 v239, v[150:153] offset:144
	ds_write_b128 v239, v[154:157] offset:160
	ds_write_b128 v239, v[158:161] offset:176
	v_mfma_f32_32x32x16_bf16 v[2:17], v[86:89], v[170:173], v[2:17]
	ds_read_b128 v[178:181], v236 offset:30208
	v_mfma_f32_32x32x16_bf16 v[18:33], v[38:41], v[170:173], v[18:33]
	ds_read_b128 v[182:185], v236 offset:30240
	v_mfma_f32_32x32x16_bf16 v[2:17], v[82:85], v[174:177], v[2:17]
	ds_read_b128 v[186:189], v236 offset:30272
	v_mfma_f32_32x32x16_bf16 v[18:33], v[34:37], v[174:177], v[18:33]
	ds_read_b128 v[190:193], v236 offset:30304
	s_waitcnt lgkmcnt(0)
	v_mfma_f32_32x32x16_bf16 v[130:145], v[94:97], v[178:181], v[194:209]
	v_mfma_f32_32x32x16_bf16 v[146:161], v[46:49], v[178:181], v[212:227]
	v_mfma_f32_32x32x16_bf16 v[130:145], v[90:93], v[182:185], v[130:145]
	v_mfma_f32_32x32x16_bf16 v[146:161], v[42:45], v[182:185], v[146:161]
	s_nop 7
	v_add_u32_e32 v239, 0x10400, v238
	ds_write_b128 v239, v[2:5] offset:0
	ds_write_b128 v239, v[6:9] offset:16
	ds_write_b128 v239, v[10:13] offset:32
	ds_write_b128 v239, v[14:17] offset:48
	ds_write_b128 v239, v[18:21] offset:128
	ds_write_b128 v239, v[22:25] offset:144
	ds_write_b128 v239, v[26:29] offset:160
	ds_write_b128 v239, v[30:33] offset:176
	v_mfma_f32_32x32x16_bf16 v[130:145], v[86:89], v[186:189], v[130:145]
	v_mfma_f32_32x32x16_bf16 v[146:161], v[38:41], v[186:189], v[146:161]
	v_mfma_f32_32x32x16_bf16 v[130:145], v[82:85], v[190:193], v[130:145]
	v_mfma_f32_32x32x16_bf16 v[146:161], v[34:37], v[190:193], v[146:161]
	s_nop 7
	s_nop 7
	v_cmp_gt_u32_e32 vcc, 16, v228
	s_and_saveexec_b64 s[20:21], vcc
	v_add_u32_e32 v239, 0x18600, v238
	ds_write_b128 v239, v[130:133] offset:0
	ds_write_b128 v239, v[134:137] offset:16
	ds_write_b128 v239, v[138:141] offset:32
	ds_write_b128 v239, v[142:145] offset:48
	ds_write_b128 v239, v[146:149] offset:128
	ds_write_b128 v239, v[150:153] offset:144
	ds_write_b128 v239, v[154:157] offset:160
	ds_write_b128 v239, v[158:161] offset:176
	s_or_b64 exec, exec, s[20:21]
	s_mov_b32 s12, 0xbeb17218
	v_mov_b32_e32 v235, 0xc038aa3b
	v_add_u32_e32 v233, v231, v244
	v_add_u32_e32 v234, v231, v245
	ds_read_b128 v[2:5], v233 offset:0
	ds_read_b128 v[6:9], v233 offset:16
	ds_read_b128 v[10:13], v233 offset:32
	ds_read_b128 v[14:17], v233 offset:48
	ds_read_b128 v[18:21], v233 offset:128
	ds_read_b128 v[22:25], v233 offset:144
	ds_read_b128 v[26:29], v233 offset:160
	ds_read_b128 v[30:33], v233 offset:176
	ds_read_b128 v[34:37], v234 offset:0
	ds_read_b128 v[38:41], v234 offset:16
	ds_read_b128 v[42:45], v234 offset:32
	ds_read_b128 v[46:49], v234 offset:48
	v_mov_b32_e32 v194, 0
	v_mov_b32_e32 v195, 0
	v_mov_b32_e32 v196, 0
	v_mov_b32_e32 v197, 0
	v_mov_b32_e32 v198, 0
	v_mov_b32_e32 v199, 0
	v_mov_b32_e32 v200, 0
	v_mov_b32_e32 v201, 0
	v_mov_b32_e32 v202, 0
	v_mov_b32_e32 v203, 0
	v_mov_b32_e32 v204, 0
	v_mov_b32_e32 v205, 0
	v_mov_b32_e32 v206, 0
	v_mov_b32_e32 v207, 0
	v_mov_b32_e32 v208, 0
	v_mov_b32_e32 v209, 0
	v_add_u32_e32 v232, 0x100, v232
	s_movk_i32 s16, 18
	s_waitcnt vmcnt(0) lgkmcnt(0)
	ds_read_b128 v[82:85], v234 offset:128
	ds_read_b128 v[86:89], v234 offset:144
	ds_read_b128 v[90:93], v234 offset:160
	ds_read_b128 v[94:97], v234 offset:176
	ds_read2_b32 v[244:245], v232 offset1:32
	v_exp_f32_e32 v212, v4
	v_exp_f32_e32 v213, v8
	v_exp_f32_e32 v214, v12
	v_exp_f32_e32 v215, v16
	v_exp_f32_e32 v217, v2
	v_fma_f32 v251, v212, s12, s12
	v_exp_f32_e32 v218, v6
	v_fma_f32 v252, v213, s12, s12
	v_exp_f32_e32 v219, v10
	v_fma_f32 v253, v214, s12, s12
	v_exp_f32_e32 v220, v14
	v_fma_f32 v254, v215, s12, s12
	v_fmac_f32_e32 v251, v217, v251
	v_fmac_f32_e32 v252, v218, v252
	v_fmac_f32_e32 v253, v219, v253
	v_fmac_f32_e32 v254, v220, v254
	v_rcp_f32_e32 v217, v251
	v_rcp_f32_e32 v218, v252
	v_rcp_f32_e32 v219, v253
	v_rcp_f32_e32 v220, v254
	v_exp_f32_e32 v246, v5
	v_fma_f32 v194, -v212, v217, v217
	v_exp_f32_e32 v247, v9
	v_fma_f32 v195, -v213, v218, v218
	v_exp_f32_e32 v248, v13
	v_fma_f32 v196, -v214, v219, v219
	v_exp_f32_e32 v249, v17
	v_fma_f32 v197, -v215, v220, v220
	v_exp_f32_e32 v212, v194
	v_add_f32_e32 v246, 1.0, v246
	v_exp_f32_e32 v213, v195
	v_add_f32_e32 v247, 1.0, v247
	v_exp_f32_e32 v214, v196
	v_add_f32_e32 v248, 1.0, v248
	v_exp_f32_e32 v215, v197
	v_add_f32_e32 v249, 1.0, v249
	v_fmac_f32_e32 v246, v246, v212
	v_fmac_f32_e32 v247, v247, v213
	v_fmac_f32_e32 v248, v248, v214
	v_fmac_f32_e32 v249, v249, v215
	v_rcp_f32_e32 v246, v246
	v_rcp_f32_e32 v247, v247
	v_rcp_f32_e32 v248, v248
	v_rcp_f32_e32 v249, v249
	v_fma_f32 v246, -v212, v246, v246
	v_fma_f32 v247, -v213, v247, v247
	v_fma_f32 v248, -v214, v248, v248
	v_fma_f32 v249, -v215, v249, v249
	v_cvt_pk_bf16_f32 v236, v246, v247
	v_cvt_pk_bf16_f32 v237, v248, v249
	s_waitcnt lgkmcnt(0)
	v_add_u32_e32 v233, v231, v244
	ds_read_b128 v[2:5], v233 offset:0
	ds_read_b128 v[6:9], v233 offset:16
	ds_read_b128 v[10:13], v233 offset:32
	ds_read_b128 v[14:17], v233 offset:48
	v_exp_f32_e32 v212, v20
	v_exp_f32_e32 v213, v24
	v_exp_f32_e32 v214, v28
	v_exp_f32_e32 v215, v32
	v_exp_f32_e32 v217, v18
	v_fma_f32 v251, v212, s12, s12
	v_exp_f32_e32 v218, v22
	v_fma_f32 v252, v213, s12, s12
	v_exp_f32_e32 v219, v26
	v_fma_f32 v253, v214, s12, s12
	v_exp_f32_e32 v220, v30
	v_fma_f32 v254, v215, s12, s12
	v_fmac_f32_e32 v251, v217, v251
	v_fmac_f32_e32 v252, v218, v252
	v_fmac_f32_e32 v253, v219, v253
	v_fmac_f32_e32 v254, v220, v254
	v_rcp_f32_e32 v217, v251
	v_rcp_f32_e32 v218, v252
	v_rcp_f32_e32 v219, v253
	v_rcp_f32_e32 v220, v254
	v_exp_f32_e32 v246, v21
	v_fma_f32 v198, -v212, v217, v217
	v_exp_f32_e32 v247, v25
	v_fma_f32 v199, -v213, v218, v218
	v_exp_f32_e32 v248, v29
	v_fma_f32 v200, -v214, v219, v219
	v_exp_f32_e32 v249, v33
	v_fma_f32 v201, -v215, v220, v220
	v_exp_f32_e32 v212, v198
	v_add_f32_e32 v246, 1.0, v246
	v_exp_f32_e32 v213, v199
	v_add_f32_e32 v247, 1.0, v247
	v_exp_f32_e32 v214, v200
	v_add_f32_e32 v248, 1.0, v248
	v_exp_f32_e32 v215, v201
	v_add_f32_e32 v249, 1.0, v249
	v_fmac_f32_e32 v246, v246, v212
	v_fmac_f32_e32 v247, v247, v213
	v_fmac_f32_e32 v248, v248, v214
	v_fmac_f32_e32 v249, v249, v215
	v_rcp_f32_e32 v246, v246
	v_rcp_f32_e32 v247, v247
	v_rcp_f32_e32 v248, v248
	v_rcp_f32_e32 v249, v249
	v_fma_f32 v246, -v212, v246, v246
	v_fma_f32 v247, -v213, v247, v247
	v_fma_f32 v248, -v214, v248, v248
	v_fma_f32 v249, -v215, v249, v249
	v_cvt_pk_bf16_f32 v238, v246, v247
	v_cvt_pk_bf16_f32 v239, v248, v249
	ds_write_b128 v211, v[236:239] offset:0
	ds_read_b128 v[18:21], v233 offset:128
	ds_read_b128 v[22:25], v233 offset:144
	ds_read_b128 v[26:29], v233 offset:160
	ds_read_b128 v[30:33], v233 offset:176
	v_exp_f32_e32 v212, v36
	v_exp_f32_e32 v213, v40
	v_exp_f32_e32 v214, v44
	v_exp_f32_e32 v215, v48
	s_waitcnt lgkmcnt(4)
	s_barrier
	ds_read_b128 v[130:133], v210 offset:0
	ds_read_b128 v[134:137], v210 offset:1024
	v_exp_f32_e32 v217, v34
	v_fma_f32 v251, v212, s12, s12
	v_exp_f32_e32 v218, v38
	v_fma_f32 v252, v213, s12, s12
	v_exp_f32_e32 v219, v42
	v_fma_f32 v253, v214, s12, s12
	v_exp_f32_e32 v220, v46
	v_fma_f32 v254, v215, s12, s12
	ds_read_b128 v[138:141], v210 offset:2048
	ds_read_b128 v[142:145], v210 offset:3072
	v_fmac_f32_e32 v251, v217, v251
	v_fmac_f32_e32 v252, v218, v252
	v_fmac_f32_e32 v253, v219, v253
	v_fmac_f32_e32 v254, v220, v254
	ds_read_b128 v[146:149], v210 offset:4096
	ds_read_b128 v[150:153], v210 offset:5120
	v_rcp_f32_e32 v217, v251
	v_rcp_f32_e32 v218, v252
	v_rcp_f32_e32 v219, v253
	v_rcp_f32_e32 v220, v254
	ds_read_b128 v[154:157], v210 offset:6144
	ds_read_b128 v[158:161], v210 offset:7168
	v_exp_f32_e32 v246, v37
	v_fma_f32 v202, -v212, v217, v217
	v_exp_f32_e32 v247, v41
	v_fma_f32 v203, -v213, v218, v218
	v_exp_f32_e32 v248, v45
	v_fma_f32 v204, -v214, v219, v219
	v_exp_f32_e32 v249, v49
	v_fma_f32 v205, -v215, v220, v220
	v_exp_f32_e32 v212, v202
	v_add_f32_e32 v246, 1.0, v246
	v_exp_f32_e32 v213, v203
	v_add_f32_e32 v247, 1.0, v247
	v_exp_f32_e32 v214, v204
	v_add_f32_e32 v248, 1.0, v248
	v_exp_f32_e32 v215, v205
	v_add_f32_e32 v249, 1.0, v249
	v_fmac_f32_e32 v246, v246, v212
	v_fmac_f32_e32 v247, v247, v213
	v_fmac_f32_e32 v248, v248, v214
	v_fmac_f32_e32 v249, v249, v215
	v_rcp_f32_e32 v246, v246
	v_rcp_f32_e32 v247, v247
	v_rcp_f32_e32 v248, v248
	v_rcp_f32_e32 v249, v249
	v_fma_f32 v246, -v212, v246, v246
	v_fma_f32 v247, -v213, v247, v247
	v_fma_f32 v248, -v214, v248, v248
	v_fma_f32 v249, -v215, v249, v249
	v_cvt_pk_bf16_f32 v236, v246, v247
	v_cvt_pk_bf16_f32 v237, v248, v249
	s_waitcnt lgkmcnt(0)
	v_mfma_f32_32x32x16_bf16 v[2:17], v[126:129], v[130:133], v[2:17]
	v_add_u32_e32 v234, v231, v245
	ds_read_b128 v[34:37], v234 offset:0
	ds_read_b128 v[38:41], v234 offset:16
	ds_read_b128 v[42:45], v234 offset:32
	ds_read_b128 v[46:49], v234 offset:48
	v_add_u32_e32 v232, 0x100, v232
	v_exp_f32_e32 v212, v84
	v_exp_f32_e32 v213, v88
	v_exp_f32_e32 v214, v92
	v_exp_f32_e32 v215, v96
	v_mfma_f32_32x32x16_bf16 v[2:17], v[122:125], v[134:137], v[2:17]
	v_exp_f32_e32 v217, v82
	v_fma_f32 v251, v212, s12, s12
	v_exp_f32_e32 v218, v86
	v_fma_f32 v252, v213, s12, s12
	v_exp_f32_e32 v219, v90
	v_fma_f32 v253, v214, s12, s12
	v_exp_f32_e32 v220, v94
	v_fma_f32 v254, v215, s12, s12
	v_mfma_f32_32x32x16_bf16 v[2:17], v[118:121], v[138:141], v[2:17]
	v_fmac_f32_e32 v251, v217, v251
	v_fmac_f32_e32 v252, v218, v252
	v_fmac_f32_e32 v253, v219, v253
	v_fmac_f32_e32 v254, v220, v254
	v_mfma_f32_32x32x16_bf16 v[2:17], v[114:117], v[142:145], v[2:17]
	v_rcp_f32_e32 v217, v251
	v_rcp_f32_e32 v218, v252
	v_rcp_f32_e32 v219, v253
	v_rcp_f32_e32 v220, v254
	v_mfma_f32_32x32x16_bf16 v[2:17], v[110:113], v[146:149], v[2:17]
	v_exp_f32_e32 v246, v85
	v_fma_f32 v206, -v212, v217, v217
	v_exp_f32_e32 v247, v89
	v_fma_f32 v207, -v213, v218, v218
	v_exp_f32_e32 v248, v93
	v_fma_f32 v208, -v214, v219, v219
	v_exp_f32_e32 v249, v97
	v_fma_f32 v209, -v215, v220, v220
	v_mfma_f32_32x32x16_bf16 v[2:17], v[106:109], v[150:153], v[2:17]
	v_mfma_f32_32x32x16_bf16 v[2:17], v[102:105], v[154:157], v[2:17]
	v_exp_f32_e32 v212, v206
	v_add_f32_e32 v246, 1.0, v246
	v_exp_f32_e32 v213, v207
	v_add_f32_e32 v247, 1.0, v247
	v_exp_f32_e32 v214, v208
	v_add_f32_e32 v248, 1.0, v248
	v_exp_f32_e32 v215, v209
	v_add_f32_e32 v249, 1.0, v249
	v_fmac_f32_e32 v246, v246, v212
	v_fmac_f32_e32 v247, v247, v213
	v_fmac_f32_e32 v248, v248, v214
	v_fmac_f32_e32 v249, v249, v215
	v_mfma_f32_32x32x16_bf16 v[2:17], v[98:101], v[158:161], v[2:17]
	v_rcp_f32_e32 v246, v246
	v_rcp_f32_e32 v247, v247
	v_rcp_f32_e32 v248, v248
	v_rcp_f32_e32 v249, v249
	v_fma_f32 v246, -v212, v246, v246
	v_fma_f32 v247, -v213, v247, v247
	v_fma_f32 v248, -v214, v248, v248
	v_fma_f32 v249, -v215, v249, v249
	v_cvt_pk_bf16_f32 v238, v246, v247
	v_cvt_pk_bf16_f32 v239, v248, v249
	ds_write_b128 v211, v[236:239] offset:8192
	.p2align 6
.Llight_loop:
	v_mfma_f32_32x32x16_bf16 v[18:33], v[78:81], v[130:133], v[18:33]
	ds_read_b128 v[82:85], v234 offset:128
	ds_read_b128 v[86:89], v234 offset:144
	ds_read_b128 v[90:93], v234 offset:160
	ds_read_b128 v[94:97], v234 offset:176
	ds_read2_b32 v[244:245], v232 offset1:32
	v_exp_f32_e32 v212, v4
	v_exp_f32_e32 v213, v8
	v_exp_f32_e32 v214, v12
	v_exp_f32_e32 v215, v16
	s_waitcnt lgkmcnt(5)
	s_barrier
	v_mfma_f32_32x32x16_bf16 v[18:33], v[74:77], v[134:137], v[18:33]
	ds_read_b128 v[162:165], v210 offset:8192
	ds_read_b128 v[166:169], v210 offset:9216
	v_exp_f32_e32 v217, v2
	v_fma_f32 v251, v212, s12, s12
	v_exp_f32_e32 v218, v6
	v_fma_f32 v252, v213, s12, s12
	v_exp_f32_e32 v219, v10
	v_fma_f32 v253, v214, s12, s12
	v_exp_f32_e32 v220, v14
	v_fma_f32 v254, v215, s12, s12
	v_mfma_f32_32x32x16_bf16 v[18:33], v[70:73], v[138:141], v[18:33]
	ds_read_b128 v[170:173], v210 offset:10240
	ds_read_b128 v[174:177], v210 offset:11264
	v_exp_f32_e32 v221, v3
	v_fmac_f32_e32 v251, v217, v251
	v_exp_f32_e32 v222, v7
	v_fmac_f32_e32 v252, v218, v252
	v_exp_f32_e32 v223, v11
	v_fmac_f32_e32 v253, v219, v253
	v_exp_f32_e32 v224, v15
	v_fmac_f32_e32 v254, v220, v254
	v_mfma_f32_32x32x16_bf16 v[18:33], v[66:69], v[142:145], v[18:33]
	ds_read_b128 v[178:181], v210 offset:12288
	ds_read_b128 v[182:185], v210 offset:13312
	v_rcp_f32_e32 v217, v251
	v_add_f32_e32 v221, 1.0, v221
	v_rcp_f32_e32 v218, v252
	v_add_f32_e32 v222, 1.0, v222
	v_rcp_f32_e32 v219, v253
	v_add_f32_e32 v223, 1.0, v223
	v_rcp_f32_e32 v220, v254
	v_add_f32_e32 v224, 1.0, v224
	v_mfma_f32_32x32x16_bf16 v[18:33], v[62:65], v[146:149], v[18:33]
	ds_read_b128 v[186:189], v210 offset:14336
	ds_read_b128 v[190:193], v210 offset:15360
	v_rcp_f32_e32 v221, v221
	v_fma_f32 v240, -v212, v217, v217
	v_rcp_f32_e32 v222, v222
	v_fma_f32 v241, -v213, v218, v218
	v_rcp_f32_e32 v223, v223
	v_fma_f32 v242, -v214, v219, v219
	v_rcp_f32_e32 v224, v224
	v_fma_f32 v243, -v215, v220, v220
	v_mfma_f32_32x32x16_bf16 v[18:33], v[58:61], v[150:153], v[18:33]
	v_exp_f32_e32 v246, v5
	v_fma_f32 v194, v221, v194, v240
	v_exp_f32_e32 v247, v9
	v_fma_f32 v195, v222, v195, v241
	v_exp_f32_e32 v248, v13
	v_fma_f32 v196, v223, v196, v242
	v_exp_f32_e32 v249, v17
	v_fma_f32 v197, v224, v197, v243
	v_mfma_f32_32x32x16_bf16 v[18:33], v[54:57], v[154:157], v[18:33]
	v_exp_f32_e32 v212, v194
	v_add_f32_e32 v246, 1.0, v246
	v_exp_f32_e32 v213, v195
	v_add_f32_e32 v247, 1.0, v247
	v_exp_f32_e32 v214, v196
	v_add_f32_e32 v248, 1.0, v248
	v_exp_f32_e32 v215, v197
	v_add_f32_e32 v249, 1.0, v249
	v_fmac_f32_e32 v246, v246, v212
	v_fmac_f32_e32 v247, v247, v213
	v_fmac_f32_e32 v248, v248, v214
	v_fmac_f32_e32 v249, v249, v215
	v_mfma_f32_32x32x16_bf16 v[18:33], v[50:53], v[158:161], v[18:33]
	v_rcp_f32_e32 v246, v246
	v_rcp_f32_e32 v247, v247
	v_rcp_f32_e32 v248, v248
	v_rcp_f32_e32 v249, v249
	v_fma_f32 v246, -v212, v246, v246
	v_fma_f32 v247, -v213, v247, v247
	v_fma_f32 v248, -v214, v248, v248
	v_fma_f32 v249, -v215, v249, v249
	v_cvt_pk_bf16_f32 v236, v246, v247
	v_cvt_pk_bf16_f32 v237, v248, v249
	s_waitcnt lgkmcnt(0)
	v_mfma_f32_32x32x16_bf16 v[34:49], v[126:129], v[162:165], v[34:49]
	v_add_u32_e32 v233, v231, v244
	ds_read_b128 v[2:5], v233 offset:0
	ds_read_b128 v[6:9], v233 offset:16
	ds_read_b128 v[10:13], v233 offset:32
	ds_read_b128 v[14:17], v233 offset:48
	v_exp_f32_e32 v212, v20
	v_exp_f32_e32 v213, v24
	v_exp_f32_e32 v214, v28
	v_exp_f32_e32 v215, v32
	v_mfma_f32_32x32x16_bf16 v[34:49], v[122:125], v[166:169], v[34:49]
	v_exp_f32_e32 v217, v18
	v_fma_f32 v251, v212, s12, s12
	v_exp_f32_e32 v218, v22
	v_fma_f32 v252, v213, s12, s12
	v_exp_f32_e32 v219, v26
	v_fma_f32 v253, v214, s12, s12
	v_exp_f32_e32 v220, v30
	v_fma_f32 v254, v215, s12, s12
	v_mfma_f32_32x32x16_bf16 v[34:49], v[118:121], v[170:173], v[34:49]
	v_exp_f32_e32 v221, v19
	v_fmac_f32_e32 v251, v217, v251
	v_exp_f32_e32 v222, v23
	v_fmac_f32_e32 v252, v218, v252
	v_exp_f32_e32 v223, v27
	v_fmac_f32_e32 v253, v219, v253
	v_exp_f32_e32 v224, v31
	v_fmac_f32_e32 v254, v220, v254
	v_mfma_f32_32x32x16_bf16 v[34:49], v[114:117], v[174:177], v[34:49]
	v_rcp_f32_e32 v217, v251
	v_add_f32_e32 v221, 1.0, v221
	v_rcp_f32_e32 v218, v252
	v_add_f32_e32 v222, 1.0, v222
	v_rcp_f32_e32 v219, v253
	v_add_f32_e32 v223, 1.0, v223
	v_rcp_f32_e32 v220, v254
	v_add_f32_e32 v224, 1.0, v224
	v_mfma_f32_32x32x16_bf16 v[34:49], v[110:113], v[178:181], v[34:49]
	v_rcp_f32_e32 v221, v221
	v_fma_f32 v240, -v212, v217, v217
	v_rcp_f32_e32 v222, v222
	v_fma_f32 v241, -v213, v218, v218
	v_rcp_f32_e32 v223, v223
	v_fma_f32 v242, -v214, v219, v219
	v_rcp_f32_e32 v224, v224
	v_fma_f32 v243, -v215, v220, v220
	v_mfma_f32_32x32x16_bf16 v[34:49], v[106:109], v[182:185], v[34:49]
	v_exp_f32_e32 v246, v21
	v_fma_f32 v198, v221, v198, v240
	v_exp_f32_e32 v247, v25
	v_fma_f32 v199, v222, v199, v241
	v_exp_f32_e32 v248, v29
	v_fma_f32 v200, v223, v200, v242
	v_exp_f32_e32 v249, v33
	v_fma_f32 v201, v224, v201, v243
	v_mfma_f32_32x32x16_bf16 v[34:49], v[102:105], v[186:189], v[34:49]
	v_exp_f32_e32 v212, v198
	v_add_f32_e32 v246, 1.0, v246
	v_exp_f32_e32 v213, v199
	v_add_f32_e32 v247, 1.0, v247
	v_exp_f32_e32 v214, v200
	v_add_f32_e32 v248, 1.0, v248
	v_exp_f32_e32 v215, v201
	v_add_f32_e32 v249, 1.0, v249
	v_fmac_f32_e32 v246, v246, v212
	v_fmac_f32_e32 v247, v247, v213
	v_fmac_f32_e32 v248, v248, v214
	v_fmac_f32_e32 v249, v249, v215
	v_mfma_f32_32x32x16_bf16 v[34:49], v[98:101], v[190:193], v[34:49]
	v_rcp_f32_e32 v246, v246
	v_rcp_f32_e32 v247, v247
	v_rcp_f32_e32 v248, v248
	v_rcp_f32_e32 v249, v249
	v_fma_f32 v246, -v212, v246, v246
	v_fma_f32 v247, -v213, v247, v247
	v_fma_f32 v248, -v214, v248, v248
	v_fma_f32 v249, -v215, v249, v249
	v_cvt_pk_bf16_f32 v238, v246, v247
	v_cvt_pk_bf16_f32 v239, v248, v249
	ds_write_b128 v211, v[236:239] offset:0
	v_mfma_f32_32x32x16_bf16 v[82:97], v[78:81], v[162:165], v[82:97]
	ds_read_b128 v[18:21], v233 offset:128
	ds_read_b128 v[22:25], v233 offset:144
	ds_read_b128 v[26:29], v233 offset:160
	ds_read_b128 v[30:33], v233 offset:176
	v_exp_f32_e32 v212, v36
	v_exp_f32_e32 v213, v40
	v_exp_f32_e32 v214, v44
	v_exp_f32_e32 v215, v48
	s_waitcnt lgkmcnt(4)
	s_barrier
	v_mfma_f32_32x32x16_bf16 v[82:97], v[74:77], v[166:169], v[82:97]
	ds_read_b128 v[130:133], v210 offset:0
	ds_read_b128 v[134:137], v210 offset:1024
	v_exp_f32_e32 v217, v34
	v_fma_f32 v251, v212, s12, s12
	v_exp_f32_e32 v218, v38
	v_fma_f32 v252, v213, s12, s12
	v_exp_f32_e32 v219, v42
	v_fma_f32 v253, v214, s12, s12
	v_exp_f32_e32 v220, v46
	v_fma_f32 v254, v215, s12, s12
	v_mfma_f32_32x32x16_bf16 v[82:97], v[70:73], v[170:173], v[82:97]
	ds_read_b128 v[138:141], v210 offset:2048
	ds_read_b128 v[142:145], v210 offset:3072
	v_exp_f32_e32 v221, v35
	v_fmac_f32_e32 v251, v217, v251
	v_exp_f32_e32 v222, v39
	v_fmac_f32_e32 v252, v218, v252
	v_exp_f32_e32 v223, v43
	v_fmac_f32_e32 v253, v219, v253
	v_exp_f32_e32 v224, v47
	v_fmac_f32_e32 v254, v220, v254
	v_mfma_f32_32x32x16_bf16 v[82:97], v[66:69], v[174:177], v[82:97]
	ds_read_b128 v[146:149], v210 offset:4096
	ds_read_b128 v[150:153], v210 offset:5120
	v_rcp_f32_e32 v217, v251
	v_add_f32_e32 v221, 1.0, v221
	v_rcp_f32_e32 v218, v252
	v_add_f32_e32 v222, 1.0, v222
	v_rcp_f32_e32 v219, v253
	v_add_f32_e32 v223, 1.0, v223
	v_rcp_f32_e32 v220, v254
	v_add_f32_e32 v224, 1.0, v224
	v_mfma_f32_32x32x16_bf16 v[82:97], v[62:65], v[178:181], v[82:97]
	ds_read_b128 v[154:157], v210 offset:6144
	ds_read_b128 v[158:161], v210 offset:7168
	v_rcp_f32_e32 v221, v221
	v_fma_f32 v240, -v212, v217, v217
	v_rcp_f32_e32 v222, v222
	v_fma_f32 v241, -v213, v218, v218
	v_rcp_f32_e32 v223, v223
	v_fma_f32 v242, -v214, v219, v219
	v_rcp_f32_e32 v224, v224
	v_fma_f32 v243, -v215, v220, v220
	v_mfma_f32_32x32x16_bf16 v[82:97], v[58:61], v[182:185], v[82:97]
	v_exp_f32_e32 v246, v37
	v_fma_f32 v202, v221, v202, v240
	v_exp_f32_e32 v247, v41
	v_fma_f32 v203, v222, v203, v241
	v_exp_f32_e32 v248, v45
	v_fma_f32 v204, v223, v204, v242
	v_exp_f32_e32 v249, v49
	v_fma_f32 v205, v224, v205, v243
	v_mfma_f32_32x32x16_bf16 v[82:97], v[54:57], v[186:189], v[82:97]
	v_exp_f32_e32 v212, v202
	v_add_f32_e32 v246, 1.0, v246
	v_exp_f32_e32 v213, v203
	v_add_f32_e32 v247, 1.0, v247
	v_exp_f32_e32 v214, v204
	v_add_f32_e32 v248, 1.0, v248
	v_exp_f32_e32 v215, v205
	v_add_f32_e32 v249, 1.0, v249
	v_fmac_f32_e32 v246, v246, v212
	v_fmac_f32_e32 v247, v247, v213
	v_fmac_f32_e32 v248, v248, v214
	v_fmac_f32_e32 v249, v249, v215
	v_mfma_f32_32x32x16_bf16 v[82:97], v[50:53], v[190:193], v[82:97]
	v_rcp_f32_e32 v246, v246
	v_rcp_f32_e32 v247, v247
	v_rcp_f32_e32 v248, v248
	v_rcp_f32_e32 v249, v249
	v_fma_f32 v246, -v212, v246, v246
	v_fma_f32 v247, -v213, v247, v247
	v_fma_f32 v248, -v214, v248, v248
	v_fma_f32 v249, -v215, v249, v249
	v_cvt_pk_bf16_f32 v236, v246, v247
	v_cvt_pk_bf16_f32 v237, v248, v249
	s_waitcnt lgkmcnt(0)
	v_mfma_f32_32x32x16_bf16 v[2:17], v[126:129], v[130:133], v[2:17]
	v_add_u32_e32 v234, v231, v245
	ds_read_b128 v[34:37], v234 offset:0
	ds_read_b128 v[38:41], v234 offset:16
	ds_read_b128 v[42:45], v234 offset:32
	ds_read_b128 v[46:49], v234 offset:48
	v_add_u32_e32 v232, 0x100, v232
	v_exp_f32_e32 v212, v84
	v_exp_f32_e32 v213, v88
	v_exp_f32_e32 v214, v92
	v_exp_f32_e32 v215, v96
	v_mfma_f32_32x32x16_bf16 v[2:17], v[122:125], v[134:137], v[2:17]
	v_exp_f32_e32 v217, v82
	v_fma_f32 v251, v212, s12, s12
	v_exp_f32_e32 v218, v86
	v_fma_f32 v252, v213, s12, s12
	v_exp_f32_e32 v219, v90
	v_fma_f32 v253, v214, s12, s12
	v_exp_f32_e32 v220, v94
	v_fma_f32 v254, v215, s12, s12
	v_mfma_f32_32x32x16_bf16 v[2:17], v[118:121], v[138:141], v[2:17]
	v_exp_f32_e32 v221, v83
	v_fmac_f32_e32 v251, v217, v251
	v_exp_f32_e32 v222, v87
	v_fmac_f32_e32 v252, v218, v252
	v_exp_f32_e32 v223, v91
	v_fmac_f32_e32 v253, v219, v253
	v_exp_f32_e32 v224, v95
	v_fmac_f32_e32 v254, v220, v254
	v_mfma_f32_32x32x16_bf16 v[2:17], v[114:117], v[142:145], v[2:17]
	v_rcp_f32_e32 v217, v251
	v_add_f32_e32 v221, 1.0, v221
	v_rcp_f32_e32 v218, v252
	v_add_f32_e32 v222, 1.0, v222
	v_rcp_f32_e32 v219, v253
	v_add_f32_e32 v223, 1.0, v223
	v_rcp_f32_e32 v220, v254
	v_add_f32_e32 v224, 1.0, v224
	v_mfma_f32_32x32x16_bf16 v[2:17], v[110:113], v[146:149], v[2:17]
	v_rcp_f32_e32 v221, v221
	v_fma_f32 v240, -v212, v217, v217
	v_rcp_f32_e32 v222, v222
	v_fma_f32 v241, -v213, v218, v218
	v_rcp_f32_e32 v223, v223
	v_fma_f32 v242, -v214, v219, v219
	v_rcp_f32_e32 v224, v224
	v_fma_f32 v243, -v215, v220, v220
	v_mfma_f32_32x32x16_bf16 v[2:17], v[106:109], v[150:153], v[2:17]
	v_exp_f32_e32 v246, v85
	v_fma_f32 v206, v221, v206, v240
	v_exp_f32_e32 v247, v89
	v_fma_f32 v207, v222, v207, v241
	v_exp_f32_e32 v248, v93
	v_fma_f32 v208, v223, v208, v242
	v_exp_f32_e32 v249, v97
	v_fma_f32 v209, v224, v209, v243
	v_mfma_f32_32x32x16_bf16 v[2:17], v[102:105], v[154:157], v[2:17]
	v_exp_f32_e32 v212, v206
	v_add_f32_e32 v246, 1.0, v246
	v_exp_f32_e32 v213, v207
	v_add_f32_e32 v247, 1.0, v247
	v_exp_f32_e32 v214, v208
	v_add_f32_e32 v248, 1.0, v248
	v_exp_f32_e32 v215, v209
	v_add_f32_e32 v249, 1.0, v249
	v_fmac_f32_e32 v246, v246, v212
	v_fmac_f32_e32 v247, v247, v213
	v_fmac_f32_e32 v248, v248, v214
	v_fmac_f32_e32 v249, v249, v215
	v_mfma_f32_32x32x16_bf16 v[2:17], v[98:101], v[158:161], v[2:17]
	v_rcp_f32_e32 v246, v246
	v_rcp_f32_e32 v247, v247
	v_rcp_f32_e32 v248, v248
	v_rcp_f32_e32 v249, v249
	v_fma_f32 v246, -v212, v246, v246
	v_fma_f32 v247, -v213, v247, v247
	v_fma_f32 v248, -v214, v248, v248
	v_fma_f32 v249, -v215, v249, v249
	v_cvt_pk_bf16_f32 v238, v246, v247
	v_cvt_pk_bf16_f32 v239, v248, v249
	ds_write_b128 v211, v[236:239] offset:8192
	s_sub_u32 s16, s16, 1
	s_cmp_lg_u32 s16, 0
	s_cbranch_scc1 .Llight_loop
	v_mfma_f32_32x32x16_bf16 v[18:33], v[78:81], v[130:133], v[18:33]
	ds_read_b128 v[82:85], v234 offset:128
	ds_read_b128 v[86:89], v234 offset:144
	ds_read_b128 v[90:93], v234 offset:160
	ds_read_b128 v[94:97], v234 offset:176
	v_exp_f32_e32 v212, v4
	v_exp_f32_e32 v213, v8
	v_exp_f32_e32 v214, v12
	v_exp_f32_e32 v215, v16
	s_waitcnt lgkmcnt(4)
	s_barrier
	v_mfma_f32_32x32x16_bf16 v[18:33], v[74:77], v[134:137], v[18:33]
	ds_read_b128 v[162:165], v210 offset:8192
	ds_read_b128 v[166:169], v210 offset:9216
	v_exp_f32_e32 v217, v2
	v_fma_f32 v251, v212, s12, s12
	v_exp_f32_e32 v218, v6
	v_fma_f32 v252, v213, s12, s12
	v_exp_f32_e32 v219, v10
	v_fma_f32 v253, v214, s12, s12
	v_exp_f32_e32 v220, v14
	v_fma_f32 v254, v215, s12, s12
	v_mfma_f32_32x32x16_bf16 v[18:33], v[70:73], v[138:141], v[18:33]
	ds_read_b128 v[170:173], v210 offset:10240
	ds_read_b128 v[174:177], v210 offset:11264
	v_exp_f32_e32 v221, v3
	v_fmac_f32_e32 v251, v217, v251
	v_exp_f32_e32 v222, v7
	v_fmac_f32_e32 v252, v218, v252
	v_exp_f32_e32 v223, v11
	v_fmac_f32_e32 v253, v219, v253
	v_exp_f32_e32 v224, v15
	v_fmac_f32_e32 v254, v220, v254
	v_mfma_f32_32x32x16_bf16 v[18:33], v[66:69], v[142:145], v[18:33]
	ds_read_b128 v[178:181], v210 offset:12288
	ds_read_b128 v[182:185], v210 offset:13312
	v_rcp_f32_e32 v217, v251
	v_add_f32_e32 v221, 1.0, v221
	v_rcp_f32_e32 v218, v252
	v_add_f32_e32 v222, 1.0, v222
	v_rcp_f32_e32 v219, v253
	v_add_f32_e32 v223, 1.0, v223
	v_rcp_f32_e32 v220, v254
	v_add_f32_e32 v224, 1.0, v224
	v_mfma_f32_32x32x16_bf16 v[18:33], v[62:65], v[146:149], v[18:33]
	ds_read_b128 v[186:189], v210 offset:14336
	ds_read_b128 v[190:193], v210 offset:15360
	v_rcp_f32_e32 v221, v221
	v_fma_f32 v240, -v212, v217, v217
	v_rcp_f32_e32 v222, v222
	v_fma_f32 v241, -v213, v218, v218
	v_rcp_f32_e32 v223, v223
	v_fma_f32 v242, -v214, v219, v219
	v_rcp_f32_e32 v224, v224
	v_fma_f32 v243, -v215, v220, v220
	v_mfma_f32_32x32x16_bf16 v[18:33], v[58:61], v[150:153], v[18:33]
	v_exp_f32_e32 v246, v5
	v_fma_f32 v194, v221, v194, v240
	v_exp_f32_e32 v247, v9
	v_fma_f32 v195, v222, v195, v241
	v_exp_f32_e32 v248, v13
	v_fma_f32 v196, v223, v196, v242
	v_exp_f32_e32 v249, v17
	v_fma_f32 v197, v224, v197, v243
	v_mfma_f32_32x32x16_bf16 v[18:33], v[54:57], v[154:157], v[18:33]
	v_exp_f32_e32 v212, v194
	v_add_f32_e32 v246, 1.0, v246
	v_exp_f32_e32 v213, v195
	v_add_f32_e32 v247, 1.0, v247
	v_exp_f32_e32 v214, v196
	v_add_f32_e32 v248, 1.0, v248
	v_exp_f32_e32 v215, v197
	v_add_f32_e32 v249, 1.0, v249
	v_fmac_f32_e32 v246, v246, v212
	v_fmac_f32_e32 v247, v247, v213
	v_fmac_f32_e32 v248, v248, v214
	v_fmac_f32_e32 v249, v249, v215
	v_mfma_f32_32x32x16_bf16 v[18:33], v[50:53], v[158:161], v[18:33]
	v_rcp_f32_e32 v246, v246
	v_rcp_f32_e32 v247, v247
	v_rcp_f32_e32 v248, v248
	v_rcp_f32_e32 v249, v249
	v_fma_f32 v246, -v212, v246, v246
	v_fma_f32 v247, -v213, v247, v247
	v_fma_f32 v248, -v214, v248, v248
	v_fma_f32 v249, -v215, v249, v249
	v_cvt_pk_bf16_f32 v236, v246, v247
	v_cvt_pk_bf16_f32 v237, v248, v249
	s_waitcnt lgkmcnt(0)
	v_mfma_f32_32x32x16_bf16 v[34:49], v[126:129], v[162:165], v[34:49]
	v_exp_f32_e32 v212, v20
	v_exp_f32_e32 v213, v24
	v_exp_f32_e32 v214, v28
	v_exp_f32_e32 v215, v32
	v_mfma_f32_32x32x16_bf16 v[34:49], v[122:125], v[166:169], v[34:49]
	v_exp_f32_e32 v217, v18
	v_fma_f32 v251, v212, s12, s12
	v_exp_f32_e32 v218, v22
	v_fma_f32 v252, v213, s12, s12
	v_exp_f32_e32 v219, v26
	v_fma_f32 v253, v214, s12, s12
	v_exp_f32_e32 v220, v30
	v_fma_f32 v254, v215, s12, s12
	v_mfma_f32_32x32x16_bf16 v[34:49], v[118:121], v[170:173], v[34:49]
	v_exp_f32_e32 v221, v19
	v_fmac_f32_e32 v251, v217, v251
	v_exp_f32_e32 v222, v23
	v_fmac_f32_e32 v252, v218, v252
	v_exp_f32_e32 v223, v27
	v_fmac_f32_e32 v253, v219, v253
	v_exp_f32_e32 v224, v31
	v_fmac_f32_e32 v254, v220, v254
	v_mfma_f32_32x32x16_bf16 v[34:49], v[114:117], v[174:177], v[34:49]
	v_rcp_f32_e32 v217, v251
	v_add_f32_e32 v221, 1.0, v221
	v_rcp_f32_e32 v218, v252
	v_add_f32_e32 v222, 1.0, v222
	v_rcp_f32_e32 v219, v253
	v_add_f32_e32 v223, 1.0, v223
	v_rcp_f32_e32 v220, v254
	v_add_f32_e32 v224, 1.0, v224
	v_mfma_f32_32x32x16_bf16 v[34:49], v[110:113], v[178:181], v[34:49]
	v_rcp_f32_e32 v221, v221
	v_fma_f32 v240, -v212, v217, v217
	v_rcp_f32_e32 v222, v222
	v_fma_f32 v241, -v213, v218, v218
	v_rcp_f32_e32 v223, v223
	v_fma_f32 v242, -v214, v219, v219
	v_rcp_f32_e32 v224, v224
	v_fma_f32 v243, -v215, v220, v220
	v_mfma_f32_32x32x16_bf16 v[34:49], v[106:109], v[182:185], v[34:49]
	v_exp_f32_e32 v246, v21
	v_fma_f32 v198, v221, v198, v240
	v_exp_f32_e32 v247, v25
	v_fma_f32 v199, v222, v199, v241
	v_exp_f32_e32 v248, v29
	v_fma_f32 v200, v223, v200, v242
	v_exp_f32_e32 v249, v33
	v_fma_f32 v201, v224, v201, v243
	v_mfma_f32_32x32x16_bf16 v[34:49], v[102:105], v[186:189], v[34:49]
	v_exp_f32_e32 v212, v198
	v_add_f32_e32 v246, 1.0, v246
	v_exp_f32_e32 v213, v199
	v_add_f32_e32 v247, 1.0, v247
	v_exp_f32_e32 v214, v200
	v_add_f32_e32 v248, 1.0, v248
	v_exp_f32_e32 v215, v201
	v_add_f32_e32 v249, 1.0, v249
	v_fmac_f32_e32 v246, v246, v212
	v_fmac_f32_e32 v247, v247, v213
	v_fmac_f32_e32 v248, v248, v214
	v_fmac_f32_e32 v249, v249, v215
	v_mfma_f32_32x32x16_bf16 v[34:49], v[98:101], v[190:193], v[34:49]
	v_rcp_f32_e32 v246, v246
	v_rcp_f32_e32 v247, v247
	v_rcp_f32_e32 v248, v248
	v_rcp_f32_e32 v249, v249
	v_fma_f32 v246, -v212, v246, v246
	v_fma_f32 v247, -v213, v247, v247
	v_fma_f32 v248, -v214, v248, v248
	v_fma_f32 v249, -v215, v249, v249
	v_cvt_pk_bf16_f32 v238, v246, v247
	v_cvt_pk_bf16_f32 v239, v248, v249
	ds_write_b128 v211, v[236:239] offset:0
	s_waitcnt lgkmcnt(0)
	s_barrier
	s_bfe_u32 s20, s19, 0x10006
	s_lshl_b32 s21, s20, 7
	s_lshl_b32 s20, s20, 13
	s_add_u32 s20, s20, 0x30000
	s_add_u32 s22, s14, s20
	s_addc_u32 s23, s15, 0
	s_add_u32 s24, s22, 0x1000
	s_addc_u32 s25, s23, 0
	global_load_dwordx4 v[98:101], v210, s[22:23] offset:0
	global_load_dwordx4 v[102:105], v210, s[22:23] offset:1024
	global_load_dwordx4 v[106:109], v210, s[22:23] offset:2048
	global_load_dwordx4 v[110:113], v210, s[22:23] offset:3072
	global_load_dwordx4 v[114:117], v210, s[24:25] offset:0
	global_load_dwordx4 v[118:121], v210, s[24:25] offset:1024
	global_load_dwordx4 v[122:125], v210, s[24:25] offset:2048
	global_load_dwordx4 v[126:129], v210, s[24:25] offset:3072
	v_or_b32_e32 v250, s21, v230
	global_load_dwordx4 v[130:133], v250, s[4:5] offset:0
	global_load_dwordx4 v[134:137], v250, s[4:5] offset:32
	global_load_dwordx4 v[138:141], v250, s[4:5] offset:64
	global_load_dwordx4 v[142:145], v250, s[4:5] offset:96
	global_load_dwordx4 v[146:149], v250, s[6:7] offset:0
	global_load_dwordx4 v[150:153], v250, s[6:7] offset:32
	global_load_dwordx4 v[154:157], v250, s[6:7] offset:64
	global_load_dwordx4 v[158:161], v250, s[6:7] offset:96
	s_load_dword s26, s[8:9], 0x0
	v_mfma_f32_32x32x16_bf16 v[82:97], v[78:81], v[162:165], v[82:97]
	v_exp_f32_e32 v212, v36
	v_exp_f32_e32 v213, v40
	v_exp_f32_e32 v214, v44
	v_exp_f32_e32 v215, v48
	v_mfma_f32_32x32x16_bf16 v[82:97], v[74:77], v[166:169], v[82:97]
	v_exp_f32_e32 v217, v34
	v_fma_f32 v251, v212, s12, s12
	v_exp_f32_e32 v218, v38
	v_fma_f32 v252, v213, s12, s12
	v_exp_f32_e32 v219, v42
	v_fma_f32 v253, v214, s12, s12
	v_exp_f32_e32 v220, v46
	v_fma_f32 v254, v215, s12, s12
	v_mfma_f32_32x32x16_bf16 v[82:97], v[70:73], v[170:173], v[82:97]
	v_exp_f32_e32 v221, v35
	v_fmac_f32_e32 v251, v217, v251
	v_exp_f32_e32 v222, v39
	v_fmac_f32_e32 v252, v218, v252
	v_exp_f32_e32 v223, v43
	v_fmac_f32_e32 v253, v219, v253
	v_exp_f32_e32 v224, v47
	v_fmac_f32_e32 v254, v220, v254
	v_mfma_f32_32x32x16_bf16 v[82:97], v[66:69], v[174:177], v[82:97]
	v_rcp_f32_e32 v217, v251
	v_add_f32_e32 v221, 1.0, v221
	v_rcp_f32_e32 v218, v252
	v_add_f32_e32 v222, 1.0, v222
	v_rcp_f32_e32 v219, v253
	v_add_f32_e32 v223, 1.0, v223
	v_rcp_f32_e32 v220, v254
	v_add_f32_e32 v224, 1.0, v224
	v_mfma_f32_32x32x16_bf16 v[82:97], v[62:65], v[178:181], v[82:97]
	v_rcp_f32_e32 v221, v221
	v_fma_f32 v240, -v212, v217, v217
	v_rcp_f32_e32 v222, v222
	v_fma_f32 v241, -v213, v218, v218
	v_rcp_f32_e32 v223, v223
	v_fma_f32 v242, -v214, v219, v219
	v_rcp_f32_e32 v224, v224
	v_fma_f32 v243, -v215, v220, v220
	v_mfma_f32_32x32x16_bf16 v[82:97], v[58:61], v[182:185], v[82:97]
	v_exp_f32_e32 v246, v37
	v_fma_f32 v202, v221, v202, v240
	v_exp_f32_e32 v247, v41
	v_fma_f32 v203, v222, v203, v241
	v_exp_f32_e32 v248, v45
	v_fma_f32 v204, v223, v204, v242
	v_exp_f32_e32 v249, v49
	v_fma_f32 v205, v224, v205, v243
	v_mfma_f32_32x32x16_bf16 v[82:97], v[54:57], v[186:189], v[82:97]
	v_exp_f32_e32 v212, v202
	v_add_f32_e32 v246, 1.0, v246
	v_exp_f32_e32 v213, v203
	v_add_f32_e32 v247, 1.0, v247
	v_exp_f32_e32 v214, v204
	v_add_f32_e32 v248, 1.0, v248
	v_exp_f32_e32 v215, v205
	v_add_f32_e32 v249, 1.0, v249
	v_fmac_f32_e32 v246, v246, v212
	v_fmac_f32_e32 v247, v247, v213
	v_fmac_f32_e32 v248, v248, v214
	v_fmac_f32_e32 v249, v249, v215
	v_mfma_f32_32x32x16_bf16 v[82:97], v[50:53], v[190:193], v[82:97]
	v_rcp_f32_e32 v246, v246
	v_rcp_f32_e32 v247, v247
	v_rcp_f32_e32 v248, v248
	v_rcp_f32_e32 v249, v249
	v_fma_f32 v246, -v212, v246, v246
	v_fma_f32 v247, -v213, v247, v247
	v_fma_f32 v248, -v214, v248, v248
	v_fma_f32 v249, -v215, v249, v249
	v_cvt_pk_bf16_f32 v236, v246, v247
	v_cvt_pk_bf16_f32 v237, v248, v249
	s_waitcnt lgkmcnt(0)
	v_exp_f32_e32 v212, v84
	v_exp_f32_e32 v213, v88
	v_exp_f32_e32 v214, v92
	v_exp_f32_e32 v215, v96
	v_exp_f32_e32 v217, v82
	v_fma_f32 v251, v212, s12, s12
	v_exp_f32_e32 v218, v86
	v_fma_f32 v252, v213, s12, s12
	v_exp_f32_e32 v219, v90
	v_fma_f32 v253, v214, s12, s12
	v_exp_f32_e32 v220, v94
	v_fma_f32 v254, v215, s12, s12
	v_exp_f32_e32 v221, v83
	v_fmac_f32_e32 v251, v217, v251
	v_exp_f32_e32 v222, v87
	v_fmac_f32_e32 v252, v218, v252
	v_exp_f32_e32 v223, v91
	v_fmac_f32_e32 v253, v219, v253
	v_exp_f32_e32 v224, v95
	v_fmac_f32_e32 v254, v220, v254
	v_rcp_f32_e32 v217, v251
	v_add_f32_e32 v221, 1.0, v221
	v_rcp_f32_e32 v218, v252
	v_add_f32_e32 v222, 1.0, v222
	v_rcp_f32_e32 v219, v253
	v_add_f32_e32 v223, 1.0, v223
	v_rcp_f32_e32 v220, v254
	v_add_f32_e32 v224, 1.0, v224
	v_rcp_f32_e32 v221, v221
	v_fma_f32 v240, -v212, v217, v217
	v_rcp_f32_e32 v222, v222
	v_fma_f32 v241, -v213, v218, v218
	v_rcp_f32_e32 v223, v223
	v_fma_f32 v242, -v214, v219, v219
	v_rcp_f32_e32 v224, v224
	v_fma_f32 v243, -v215, v220, v220
	v_exp_f32_e32 v246, v85
	v_fma_f32 v206, v221, v206, v240
	v_exp_f32_e32 v247, v89
	v_fma_f32 v207, v222, v207, v241
	v_exp_f32_e32 v248, v93
	v_fma_f32 v208, v223, v208, v242
	v_exp_f32_e32 v249, v97
	v_fma_f32 v209, v224, v209, v243
	v_exp_f32_e32 v212, v206
	v_add_f32_e32 v246, 1.0, v246
	v_exp_f32_e32 v213, v207
	v_add_f32_e32 v247, 1.0, v247
	v_exp_f32_e32 v214, v208
	v_add_f32_e32 v248, 1.0, v248
	v_exp_f32_e32 v215, v209
	v_add_f32_e32 v249, 1.0, v249
	v_fmac_f32_e32 v246, v246, v212
	v_fmac_f32_e32 v247, v247, v213
	v_fmac_f32_e32 v248, v248, v214
	v_fmac_f32_e32 v249, v249, v215
	v_rcp_f32_e32 v246, v246
	v_rcp_f32_e32 v247, v247
	v_rcp_f32_e32 v248, v248
	v_rcp_f32_e32 v249, v249
	v_fma_f32 v246, -v212, v246, v246
	v_fma_f32 v247, -v213, v247, v247
	v_fma_f32 v248, -v214, v248, v248
	v_fma_f32 v249, -v215, v249, v249
	v_cvt_pk_bf16_f32 v238, v246, v247
	v_cvt_pk_bf16_f32 v239, v248, v249
	ds_write_b128 v211, v[236:239] offset:8192
	s_waitcnt lgkmcnt(0)
	s_barrier
	s_lshl_b32 s20, s19, 6
	s_and_b32 s20, s20, 0x2000
	v_or_b32_e32 v20, s20, v210
	ds_read_b128 v[162:165], v20 offset:0
	ds_read_b128 v[166:169], v20 offset:1024
	ds_read_b128 v[170:173], v20 offset:2048
	ds_read_b128 v[174:177], v20 offset:3072
	ds_read_b128 v[178:181], v20 offset:4096
	ds_read_b128 v[182:185], v20 offset:5120
	ds_read_b128 v[186:189], v20 offset:6144
	ds_read_b128 v[190:193], v20 offset:7168
	s_bfe_u32 s20, s19, 0x10006
	s_lshl_b32 s20, s20, 9
	s_and_b32 s21, s19, 0x80
	s_or_b32 s20, s20, s21
	v_lshlrev_b32_e32 v19, 2, v229
	v_add3_u32 v19, s20, v19, v228
	s_waitcnt vmcnt(0)
	s_waitcnt lgkmcnt(7)
	v_mfma_f32_32x32x16_bf16 v[2:17], v[98:101], v[162:165], 0
	s_waitcnt lgkmcnt(6)
	v_mfma_f32_32x32x16_bf16 v[2:17], v[102:105], v[166:169], v[2:17]
	s_waitcnt lgkmcnt(5)
	v_mfma_f32_32x32x16_bf16 v[2:17], v[106:109], v[170:173], v[2:17]
	s_waitcnt lgkmcnt(4)
	v_mfma_f32_32x32x16_bf16 v[2:17], v[110:113], v[174:177], v[2:17]
	s_waitcnt lgkmcnt(3)
	v_mfma_f32_32x32x16_bf16 v[2:17], v[114:117], v[178:181], v[2:17]
	s_waitcnt lgkmcnt(2)
	v_mfma_f32_32x32x16_bf16 v[2:17], v[118:121], v[182:185], v[2:17]
	s_waitcnt lgkmcnt(1)
	v_mfma_f32_32x32x16_bf16 v[2:17], v[122:125], v[186:189], v[2:17]
	s_waitcnt lgkmcnt(0)
	v_mfma_f32_32x32x16_bf16 v[2:17], v[126:129], v[190:193], v[2:17]
	s_nop 15
	s_nop 3
	v_add_f32_e32 v2, v2, v130
	v_add_f32_e32 v3, v3, v131
	v_add_f32_e32 v4, v4, v132
	v_add_f32_e32 v5, v5, v133
	v_add_f32_e32 v6, v6, v134
	v_add_f32_e32 v7, v7, v135
	v_add_f32_e32 v8, v8, v136
	v_add_f32_e32 v9, v9, v137
	v_add_f32_e32 v10, v10, v138
	v_add_f32_e32 v11, v11, v139
	v_add_f32_e32 v12, v12, v140
	v_add_f32_e32 v13, v13, v141
	v_add_f32_e32 v14, v14, v142
	v_add_f32_e32 v15, v15, v143
	v_add_f32_e32 v16, v16, v144
	v_add_f32_e32 v17, v17, v145
	v_max_f32_e32 v2, 0, v2
	v_max_f32_e32 v3, 0, v3
	v_max_f32_e32 v4, 0, v4
	v_max_f32_e32 v5, 0, v5
	v_max_f32_e32 v6, 0, v6
	v_max_f32_e32 v7, 0, v7
	v_max_f32_e32 v8, 0, v8
	v_max_f32_e32 v9, 0, v9
	v_max_f32_e32 v10, 0, v10
	v_max_f32_e32 v11, 0, v11
	v_max_f32_e32 v12, 0, v12
	v_max_f32_e32 v13, 0, v13
	v_max_f32_e32 v14, 0, v14
	v_max_f32_e32 v15, 0, v15
	v_max_f32_e32 v16, 0, v16
	v_max_f32_e32 v17, 0, v17
	v_fma_f32 v18, v2, v146, 0
	v_fmac_f32_e32 v18, v3, v147
	v_fmac_f32_e32 v18, v4, v148
	v_fmac_f32_e32 v18, v5, v149
	v_fmac_f32_e32 v18, v6, v150
	v_fmac_f32_e32 v18, v7, v151
	v_fmac_f32_e32 v18, v8, v152
	v_fmac_f32_e32 v18, v9, v153
	v_fmac_f32_e32 v18, v10, v154
	v_fmac_f32_e32 v18, v11, v155
	v_fmac_f32_e32 v18, v12, v156
	v_fmac_f32_e32 v18, v13, v157
	v_fmac_f32_e32 v18, v14, v158
	v_fmac_f32_e32 v18, v15, v159
	v_fmac_f32_e32 v18, v16, v160
	v_fmac_f32_e32 v18, v17, v161
	ds_write_b32 v19, v18 offset:35904
	s_branch .LBB1_40
